# baseline (speedup 1.0000x reference)
attn_fwd_pwg4x64:
	s_load_dwordx2 s[22:23], s[0:1], 0x0
	s_load_dwordx8 s[4:11], s[0:1], 0x8
	s_load_dwordx2 s[36:37], s[0:1], 0x28
	s_load_dwordx4 s[16:19], s[0:1], 0x30
	s_load_dwordx2 s[20:21], s[0:1], 0x40
	s_and_b32 s3, s2, 15
	s_bfe_u32 s30, s2, 0x30004
	s_lshr_b32 s2, s2, 3
	s_and_b32 s2, s2, 0x1ffffff0
	s_or_b32 s2, s2, s3
	s_mov_b32 s3, 0
	s_lshl_b32 s31, s30, 8
	s_lshl_b64 s[26:27], s[2:3], 19
	s_lshl_b64 s[24:25], s[2:3], 11
	s_lshl_b64 s[38:39], s[2:3], 20
	s_lshl_b32 s43, s30, 17
	s_add_u32 s38, s38, s43
	s_addc_u32 s39, s39, 0
	v_and_b32_e32 v1, 15, v0
	v_lshrrev_b32_e32 v28, 4, v0
	v_lshrrev_b32_e32 v29, 6, v0
	v_lshlrev_b32_e32 v30, 5, v1
	v_lshl_or_b32 v2, v28, 9, v30
	v_bfe_u32 v31, v0, 4, 2
	v_lshl_or_b32 v3, v31, 9, v30
	v_lshl_or_b32 v3, v29, 15, v3
	v_lshlrev_b32_e32 v32, 4, v1
	v_lshl_or_b32 v26, v28, 8, v32
	s_lshl_b32 s43, s30, 16
	v_or_b32_e32 v26, s43, v26
	v_lshlrev_b32_e32 v38, 2, v0
	v_lshlrev_b32_e32 v40, 14, v29
	v_lshlrev_b32_e32 v33, 12, v29
	v_mbcnt_lo_u32_b32 v39, -1, 0
	v_mbcnt_hi_u32_b32 v39, -1, v39
	v_readfirstlane_b32 s28, v33
	v_readfirstlane_b32 s29, v33
	v_mov_b32_e32 v200, 0
	v_mov_b32_e32 v201, 0
	v_mov_b32_e32 v202, 0
	v_mov_b32_e32 v203, 0
	v_mov_b32_e32 v204, 0
	v_mov_b32_e32 v205, 0
	v_mov_b32_e32 v206, 0
	v_mov_b32_e32 v207, 0
	s_mov_b32 s44, 0x3e0293ee
	s_mov_b32 s45, 0x3e0293ee
	s_waitcnt lgkmcnt(0)
	s_add_u32 s12, s4, s26
	s_addc_u32 s13, s5, s27
	s_and_b32 s13, s13, 0xffff
	s_mov_b32 s14, 0x80000
	s_mov_b32 s15, 0x20000
	s_add_u32 s4, s6, s26
	s_addc_u32 s5, s7, s27
	s_and_b32 s5, s5, 0xffff
	s_mov_b32 s6, 0x80000
	s_mov_b32 s7, 0x20000
	s_add_u32 s32, s10, s38
	s_addc_u32 s33, s11, s39
	s_add_u32 s34, s36, s38
	s_addc_u32 s35, s37, s39
	s_lshl_b32 s43, s30, 17
	s_sub_u32 s80, s34, s43
	s_subb_u32 s81, s35, 0
	s_and_b32 s81, s81, 0xffff
	s_mov_b32 s82, 0x100000
	s_mov_b32 s83, 0x20000
	s_add_i32 s86, s43, 0x8000
	s_add_u32 s40, s22, s38
	s_addc_u32 s41, s23, s39
	s_lshl_b64 s[46:47], s[2:3], 5
	s_add_u32 s10, s16, s46
	s_addc_u32 s11, s17, s47
	s_lshl_b32 s43, s30, 2
	s_add_u32 s46, s10, s43
	s_addc_u32 s47, s11, 0
	s_lshl_b64 s[26:27], s[2:3], 12
	s_add_u32 s26, s18, s26
	s_addc_u32 s27, s19, s27
	s_lshl_b32 s43, s30, 9
	s_add_u32 s26, s26, s43
	s_addc_u32 s27, s27, 0
	global_load_dwordx4 v[42:45], v2, s[32:33] nt
	global_load_dwordx4 v[46:49], v2, s[32:33] offset:16 nt
	s_add_u32 s32, s32, 8192
	s_addc_u32 s33, s33, 0
	global_load_dwordx4 v[50:53], v2, s[32:33] nt
	global_load_dwordx4 v[54:57], v2, s[32:33] offset:16 nt
	s_add_u32 s32, s32, 8192
	s_addc_u32 s33, s33, 0
	global_load_dwordx4 v[68:71], v2, s[32:33] nt
	global_load_dwordx4 v[72:75], v2, s[32:33] offset:16 nt
	s_add_u32 s32, s32, 8192
	s_addc_u32 s33, s33, 0
	global_load_dwordx4 v[76:79], v2, s[32:33] nt
	global_load_dwordx4 v[80:83], v2, s[32:33] offset:16 nt
	s_add_u32 s32, s32, 8192
	s_addc_u32 s33, s33, 0
	global_load_dwordx4 v[248:251], v2, s[32:33] nt
	global_load_dwordx4 v[252:255], v2, s[32:33] offset:16 nt
	s_add_u32 s32, s32, 8192
	s_addc_u32 s33, s33, 0
	global_load_dwordx4 v[84:87], v2, s[34:35] nt
	global_load_dwordx4 v[88:91], v2, s[34:35] offset:16 nt
	s_add_u32 s34, s34, 8192
	s_addc_u32 s35, s35, 0
	global_load_dwordx4 v[92:95], v2, s[34:35] nt
	global_load_dwordx4 v[96:99], v2, s[34:35] offset:16 nt
	s_add_u32 s34, s34, 8192
	s_addc_u32 s35, s35, 0
	global_load_dwordx4 v[100:103], v2, s[34:35] nt
	global_load_dwordx4 v[104:107], v2, s[34:35] offset:16 nt
	s_add_u32 s34, s34, 8192
	s_addc_u32 s35, s35, 0
	global_load_dwordx4 v[108:111], v2, s[34:35] nt
	global_load_dwordx4 v[112:115], v2, s[34:35] offset:16 nt
	s_add_u32 s34, s34, 8192
	s_addc_u32 s35, s35, 0
	global_load_dwordx4 v[116:119], v3, s[40:41] nt
	global_load_dwordx4 v[120:123], v3, s[40:41] offset:16 nt
	s_add_u32 s40, s40, 2048
	s_addc_u32 s41, s41, 0
	global_load_dwordx4 v[124:127], v3, s[40:41] nt
	global_load_dwordx4 v[128:131], v3, s[40:41] offset:16 nt
	s_add_u32 s40, s40, 2048
	s_addc_u32 s41, s41, 0
	global_load_dwordx4 v[132:135], v3, s[40:41] nt
	global_load_dwordx4 v[136:139], v3, s[40:41] offset:16 nt
	s_add_u32 s40, s40, 2048
	s_addc_u32 s41, s41, 0
	global_load_dwordx4 v[140:143], v3, s[40:41] nt
	global_load_dwordx4 v[144:147], v3, s[40:41] offset:16 nt
	s_add_u32 s40, s40, 2048
	s_addc_u32 s41, s41, 0
	global_load_dwordx4 v[148:151], v3, s[40:41] nt
	global_load_dwordx4 v[152:155], v3, s[40:41] offset:16 nt
	s_add_u32 s40, s40, 2048
	s_addc_u32 s41, s41, 0
	global_load_dwordx4 v[156:159], v3, s[40:41] nt
	global_load_dwordx4 v[160:163], v3, s[40:41] offset:16 nt
	s_add_u32 s40, s40, 2048
	s_addc_u32 s41, s41, 0
	global_load_dwordx4 v[164:167], v3, s[40:41] nt
	global_load_dwordx4 v[168:171], v3, s[40:41] offset:16 nt
	s_add_u32 s40, s40, 2048
	s_addc_u32 s41, s41, 0
	global_load_dwordx4 v[172:175], v3, s[40:41] nt
	global_load_dwordx4 v[176:179], v3, s[40:41] offset:16 nt
	s_add_u32 s40, s40, 2048
	s_addc_u32 s41, s41, 0
	s_waitcnt vmcnt(32)
	v_cvt_pk_bf16_f32 v12, v42, v43
	v_cvt_pk_bf16_f32 v13, v44, v45
	v_cvt_pk_bf16_f32 v14, v46, v47
	v_cvt_pk_bf16_f32 v15, v48, v49
	s_mov_b32 s42, 0x0
	buffer_store_dwordx4 v[12:15], v26, s[12:15], s42 offen sc1
	global_load_dwordx4 v[42:45], v3, s[40:41] nt
	global_load_dwordx4 v[46:49], v3, s[40:41] offset:16 nt
	s_add_u32 s40, s40, 2048
	s_addc_u32 s41, s41, 0
	s_waitcnt vmcnt(33)
	v_cvt_pk_bf16_f32 v16, v50, v51
	v_cvt_pk_bf16_f32 v17, v52, v53
	v_cvt_pk_bf16_f32 v18, v54, v55
	v_cvt_pk_bf16_f32 v19, v56, v57
	s_mov_b32 s42, 0x1000
	buffer_store_dwordx4 v[16:19], v26, s[12:15], s42 offen sc1
	global_load_dwordx4 v[50:53], v3, s[40:41] nt
	global_load_dwordx4 v[54:57], v3, s[40:41] offset:16 nt
	s_add_u32 s40, s40, 2048
	s_addc_u32 s41, s41, 0
	s_waitcnt vmcnt(34)
	v_cvt_pk_bf16_f32 v20, v68, v69
	v_cvt_pk_bf16_f32 v21, v70, v71
	v_cvt_pk_bf16_f32 v22, v72, v73
	v_cvt_pk_bf16_f32 v23, v74, v75
	s_mov_b32 s42, 0x2000
	buffer_store_dwordx4 v[20:23], v26, s[12:15], s42 offen sc1
	global_load_dwordx4 v[68:71], v3, s[40:41] nt
	global_load_dwordx4 v[72:75], v3, s[40:41] offset:16 nt
	s_add_u32 s40, s40, 2048
	s_addc_u32 s41, s41, 0
	s_waitcnt vmcnt(35)
	v_cvt_pk_bf16_f32 v12, v76, v77
	v_cvt_pk_bf16_f32 v13, v78, v79
	v_cvt_pk_bf16_f32 v14, v80, v81
	v_cvt_pk_bf16_f32 v15, v82, v83
	s_mov_b32 s42, 0x3000
	buffer_store_dwordx4 v[12:15], v26, s[12:15], s42 offen sc1
	global_load_dwordx4 v[76:79], v3, s[40:41] nt
	global_load_dwordx4 v[80:83], v3, s[40:41] offset:16 nt
	s_add_u32 s40, s40, 2048
	s_addc_u32 s41, s41, 0
	s_waitcnt vmcnt(34)
	v_pk_add_f32 v[200:201], v[84:85], v[200:201]
	v_pk_add_f32 v[202:203], v[86:87], v[202:203]
	v_pk_add_f32 v[204:205], v[88:89], v[204:205]
	v_pk_add_f32 v[206:207], v[90:91], v[206:207]
	v_cvt_pk_bf16_f32 v16, v84, v85
	v_cvt_pk_bf16_f32 v17, v86, v87
	v_cvt_pk_bf16_f32 v18, v88, v89
	v_cvt_pk_bf16_f32 v19, v90, v91
	s_mov_b32 s42, 0x0
	buffer_store_dwordx4 v[16:19], v26, s[4:7], s42 offen sc1
	global_load_dwordx4 v[84:87], v3, s[40:41] nt
	global_load_dwordx4 v[88:91], v3, s[40:41] offset:16 nt
	s_add_u32 s40, s40, 2048
	s_addc_u32 s41, s41, 0
	s_waitcnt vmcnt(35)
	v_pk_add_f32 v[200:201], v[92:93], v[200:201]
	v_pk_add_f32 v[202:203], v[94:95], v[202:203]
	v_pk_add_f32 v[204:205], v[96:97], v[204:205]
	v_pk_add_f32 v[206:207], v[98:99], v[206:207]
	v_cvt_pk_bf16_f32 v20, v92, v93
	v_cvt_pk_bf16_f32 v21, v94, v95
	v_cvt_pk_bf16_f32 v22, v96, v97
	v_cvt_pk_bf16_f32 v23, v98, v99
	s_mov_b32 s42, 0x1000
	buffer_store_dwordx4 v[20:23], v26, s[4:7], s42 offen sc1
	global_load_dwordx4 v[92:95], v3, s[40:41] nt
	global_load_dwordx4 v[96:99], v3, s[40:41] offset:16 nt
	s_add_u32 s40, s40, 2048
	s_addc_u32 s41, s41, 0
	s_waitcnt vmcnt(36)
	v_pk_add_f32 v[200:201], v[100:101], v[200:201]
	v_pk_add_f32 v[202:203], v[102:103], v[202:203]
	v_pk_add_f32 v[204:205], v[104:105], v[204:205]
	v_pk_add_f32 v[206:207], v[106:107], v[206:207]
	v_cvt_pk_bf16_f32 v12, v100, v101
	v_cvt_pk_bf16_f32 v13, v102, v103
	v_cvt_pk_bf16_f32 v14, v104, v105
	v_cvt_pk_bf16_f32 v15, v106, v107
	s_mov_b32 s42, 0x2000
	buffer_store_dwordx4 v[12:15], v26, s[4:7], s42 offen sc1
	global_load_dwordx4 v[100:103], v3, s[40:41] nt
	global_load_dwordx4 v[104:107], v3, s[40:41] offset:16 nt
	s_add_u32 s40, s40, 2048
	s_addc_u32 s41, s41, 0
	s_waitcnt vmcnt(37)
	v_pk_add_f32 v[200:201], v[108:109], v[200:201]
	v_pk_add_f32 v[202:203], v[110:111], v[202:203]
	v_pk_add_f32 v[204:205], v[112:113], v[204:205]
	v_pk_add_f32 v[206:207], v[114:115], v[206:207]
	v_cvt_pk_bf16_f32 v16, v108, v109
	v_cvt_pk_bf16_f32 v17, v110, v111
	v_cvt_pk_bf16_f32 v18, v112, v113
	v_cvt_pk_bf16_f32 v19, v114, v115
	s_mov_b32 s42, 0x3000
	buffer_store_dwordx4 v[16:19], v26, s[4:7], s42 offen sc1
	global_load_dwordx4 v[108:111], v3, s[40:41] nt
	global_load_dwordx4 v[112:115], v3, s[40:41] offset:16 nt
	s_add_u32 s40, s40, 2048
	s_addc_u32 s41, s41, 0
	v_lshrrev_b32_e32 v37, 4, v39
	v_and_b32_e32 v26, 15, v39
	v_xor_b32_e32 v27, v26, v37
	v_xor_b32_e32 v28, 4, v27
	v_lshlrev_b32_e32 v29, 8, v37
	v_or_b32_e32 v36, 0x10000, v40
	v_add_u32_e32 v29, v29, v36
	v_lshl_add_u32 v24, v27, 4, v29
	v_lshl_add_u32 v25, v28, 4, v29
	s_waitcnt vmcnt(38)
	v_pk_mul_f32 v[116:117], v[116:117], s[44:45] op_sel_hi:[1,0]
	v_pk_mul_f32 v[118:119], v[118:119], s[44:45] op_sel_hi:[1,0]
	v_pk_mul_f32 v[120:121], v[120:121], s[44:45] op_sel_hi:[1,0]
	v_pk_mul_f32 v[122:123], v[122:123], s[44:45] op_sel_hi:[1,0]
	v_cvt_pk_bf16_f32 v12, v116, v117
	v_cvt_pk_bf16_f32 v13, v118, v119
	v_cvt_pk_bf16_f32 v14, v120, v121
	v_cvt_pk_bf16_f32 v15, v122, v123
	ds_write_b128 v24, v[12:15] offset:0
	s_waitcnt vmcnt(36)
	v_pk_mul_f32 v[124:125], v[124:125], s[44:45] op_sel_hi:[1,0]
	v_pk_mul_f32 v[126:127], v[126:127], s[44:45] op_sel_hi:[1,0]
	v_pk_mul_f32 v[128:129], v[128:129], s[44:45] op_sel_hi:[1,0]
	v_pk_mul_f32 v[130:131], v[130:131], s[44:45] op_sel_hi:[1,0]
	v_cvt_pk_bf16_f32 v16, v124, v125
	v_cvt_pk_bf16_f32 v17, v126, v127
	v_cvt_pk_bf16_f32 v18, v128, v129
	v_cvt_pk_bf16_f32 v19, v130, v131
	ds_write_b128 v25, v[16:19] offset:1024
	s_waitcnt vmcnt(34)
	v_pk_mul_f32 v[132:133], v[132:133], s[44:45] op_sel_hi:[1,0]
	v_pk_mul_f32 v[134:135], v[134:135], s[44:45] op_sel_hi:[1,0]
	v_pk_mul_f32 v[136:137], v[136:137], s[44:45] op_sel_hi:[1,0]
	v_pk_mul_f32 v[138:139], v[138:139], s[44:45] op_sel_hi:[1,0]
	v_cvt_pk_bf16_f32 v20, v132, v133
	v_cvt_pk_bf16_f32 v21, v134, v135
	v_cvt_pk_bf16_f32 v22, v136, v137
	v_cvt_pk_bf16_f32 v23, v138, v139
	ds_write_b128 v24, v[20:23] offset:2048
	s_waitcnt vmcnt(32)
	v_pk_mul_f32 v[140:141], v[140:141], s[44:45] op_sel_hi:[1,0]
	v_pk_mul_f32 v[142:143], v[142:143], s[44:45] op_sel_hi:[1,0]
	v_pk_mul_f32 v[144:145], v[144:145], s[44:45] op_sel_hi:[1,0]
	v_pk_mul_f32 v[146:147], v[146:147], s[44:45] op_sel_hi:[1,0]
	v_cvt_pk_bf16_f32 v12, v140, v141
	v_cvt_pk_bf16_f32 v13, v142, v143
	v_cvt_pk_bf16_f32 v14, v144, v145
	v_cvt_pk_bf16_f32 v15, v146, v147
	ds_write_b128 v25, v[12:15] offset:3072
	s_waitcnt vmcnt(30)
	v_pk_mul_f32 v[148:149], v[148:149], s[44:45] op_sel_hi:[1,0]
	v_pk_mul_f32 v[150:151], v[150:151], s[44:45] op_sel_hi:[1,0]
	v_pk_mul_f32 v[152:153], v[152:153], s[44:45] op_sel_hi:[1,0]
	v_pk_mul_f32 v[154:155], v[154:155], s[44:45] op_sel_hi:[1,0]
	v_cvt_pk_bf16_f32 v16, v148, v149
	v_cvt_pk_bf16_f32 v17, v150, v151
	v_cvt_pk_bf16_f32 v18, v152, v153
	v_cvt_pk_bf16_f32 v19, v154, v155
	ds_write_b128 v24, v[16:19] offset:4096
	s_waitcnt vmcnt(28)
	v_pk_mul_f32 v[156:157], v[156:157], s[44:45] op_sel_hi:[1,0]
	v_pk_mul_f32 v[158:159], v[158:159], s[44:45] op_sel_hi:[1,0]
	v_pk_mul_f32 v[160:161], v[160:161], s[44:45] op_sel_hi:[1,0]
	v_pk_mul_f32 v[162:163], v[162:163], s[44:45] op_sel_hi:[1,0]
	v_cvt_pk_bf16_f32 v20, v156, v157
	v_cvt_pk_bf16_f32 v21, v158, v159
	v_cvt_pk_bf16_f32 v22, v160, v161
	v_cvt_pk_bf16_f32 v23, v162, v163
	ds_write_b128 v25, v[20:23] offset:5120
	s_waitcnt vmcnt(26)
	v_pk_mul_f32 v[164:165], v[164:165], s[44:45] op_sel_hi:[1,0]
	v_pk_mul_f32 v[166:167], v[166:167], s[44:45] op_sel_hi:[1,0]
	v_pk_mul_f32 v[168:169], v[168:169], s[44:45] op_sel_hi:[1,0]
	v_pk_mul_f32 v[170:171], v[170:171], s[44:45] op_sel_hi:[1,0]
	v_cvt_pk_bf16_f32 v12, v164, v165
	v_cvt_pk_bf16_f32 v13, v166, v167
	v_cvt_pk_bf16_f32 v14, v168, v169
	v_cvt_pk_bf16_f32 v15, v170, v171
	ds_write_b128 v24, v[12:15] offset:6144
	s_waitcnt vmcnt(24)
	v_pk_mul_f32 v[172:173], v[172:173], s[44:45] op_sel_hi:[1,0]
	v_pk_mul_f32 v[174:175], v[174:175], s[44:45] op_sel_hi:[1,0]
	v_pk_mul_f32 v[176:177], v[176:177], s[44:45] op_sel_hi:[1,0]
	v_pk_mul_f32 v[178:179], v[178:179], s[44:45] op_sel_hi:[1,0]
	v_cvt_pk_bf16_f32 v16, v172, v173
	v_cvt_pk_bf16_f32 v17, v174, v175
	v_cvt_pk_bf16_f32 v18, v176, v177
	v_cvt_pk_bf16_f32 v19, v178, v179
	ds_write_b128 v25, v[16:19] offset:7168
	s_waitcnt vmcnt(21)
	v_pk_mul_f32 v[42:43], v[42:43], s[44:45] op_sel_hi:[1,0]
	v_pk_mul_f32 v[44:45], v[44:45], s[44:45] op_sel_hi:[1,0]
	v_pk_mul_f32 v[46:47], v[46:47], s[44:45] op_sel_hi:[1,0]
	v_pk_mul_f32 v[48:49], v[48:49], s[44:45] op_sel_hi:[1,0]
	v_cvt_pk_bf16_f32 v20, v42, v43
	v_cvt_pk_bf16_f32 v21, v44, v45
	v_cvt_pk_bf16_f32 v22, v46, v47
	v_cvt_pk_bf16_f32 v23, v48, v49
	ds_write_b128 v24, v[20:23] offset:8192
	s_waitcnt vmcnt(18)
	v_pk_mul_f32 v[50:51], v[50:51], s[44:45] op_sel_hi:[1,0]
	v_pk_mul_f32 v[52:53], v[52:53], s[44:45] op_sel_hi:[1,0]
	v_pk_mul_f32 v[54:55], v[54:55], s[44:45] op_sel_hi:[1,0]
	v_pk_mul_f32 v[56:57], v[56:57], s[44:45] op_sel_hi:[1,0]
	v_cvt_pk_bf16_f32 v12, v50, v51
	v_cvt_pk_bf16_f32 v13, v52, v53
	v_cvt_pk_bf16_f32 v14, v54, v55
	v_cvt_pk_bf16_f32 v15, v56, v57
	ds_write_b128 v25, v[12:15] offset:9216
	s_waitcnt vmcnt(15)
	v_pk_mul_f32 v[68:69], v[68:69], s[44:45] op_sel_hi:[1,0]
	v_pk_mul_f32 v[70:71], v[70:71], s[44:45] op_sel_hi:[1,0]
	v_pk_mul_f32 v[72:73], v[72:73], s[44:45] op_sel_hi:[1,0]
	v_pk_mul_f32 v[74:75], v[74:75], s[44:45] op_sel_hi:[1,0]
	v_cvt_pk_bf16_f32 v16, v68, v69
	v_cvt_pk_bf16_f32 v17, v70, v71
	v_cvt_pk_bf16_f32 v18, v72, v73
	v_cvt_pk_bf16_f32 v19, v74, v75
	ds_write_b128 v24, v[16:19] offset:10240
	s_waitcnt vmcnt(12)
	v_pk_mul_f32 v[76:77], v[76:77], s[44:45] op_sel_hi:[1,0]
	v_pk_mul_f32 v[78:79], v[78:79], s[44:45] op_sel_hi:[1,0]
	v_pk_mul_f32 v[80:81], v[80:81], s[44:45] op_sel_hi:[1,0]
	v_pk_mul_f32 v[82:83], v[82:83], s[44:45] op_sel_hi:[1,0]
	v_cvt_pk_bf16_f32 v20, v76, v77
	v_cvt_pk_bf16_f32 v21, v78, v79
	v_cvt_pk_bf16_f32 v22, v80, v81
	v_cvt_pk_bf16_f32 v23, v82, v83
	ds_write_b128 v25, v[20:23] offset:11264
	s_waitcnt vmcnt(9)
	v_pk_mul_f32 v[84:85], v[84:85], s[44:45] op_sel_hi:[1,0]
	v_pk_mul_f32 v[86:87], v[86:87], s[44:45] op_sel_hi:[1,0]
	v_pk_mul_f32 v[88:89], v[88:89], s[44:45] op_sel_hi:[1,0]
	v_pk_mul_f32 v[90:91], v[90:91], s[44:45] op_sel_hi:[1,0]
	v_cvt_pk_bf16_f32 v12, v84, v85
	v_cvt_pk_bf16_f32 v13, v86, v87
	v_cvt_pk_bf16_f32 v14, v88, v89
	v_cvt_pk_bf16_f32 v15, v90, v91
	ds_write_b128 v24, v[12:15] offset:12288
	s_waitcnt vmcnt(6)
	v_pk_mul_f32 v[92:93], v[92:93], s[44:45] op_sel_hi:[1,0]
	v_pk_mul_f32 v[94:95], v[94:95], s[44:45] op_sel_hi:[1,0]
	v_pk_mul_f32 v[96:97], v[96:97], s[44:45] op_sel_hi:[1,0]
	v_pk_mul_f32 v[98:99], v[98:99], s[44:45] op_sel_hi:[1,0]
	v_cvt_pk_bf16_f32 v16, v92, v93
	v_cvt_pk_bf16_f32 v17, v94, v95
	v_cvt_pk_bf16_f32 v18, v96, v97
	v_cvt_pk_bf16_f32 v19, v98, v99
	ds_write_b128 v25, v[16:19] offset:13312
	s_waitcnt vmcnt(3)
	v_pk_mul_f32 v[100:101], v[100:101], s[44:45] op_sel_hi:[1,0]
	v_pk_mul_f32 v[102:103], v[102:103], s[44:45] op_sel_hi:[1,0]
	v_pk_mul_f32 v[104:105], v[104:105], s[44:45] op_sel_hi:[1,0]
	v_pk_mul_f32 v[106:107], v[106:107], s[44:45] op_sel_hi:[1,0]
	v_cvt_pk_bf16_f32 v20, v100, v101
	v_cvt_pk_bf16_f32 v21, v102, v103
	v_cvt_pk_bf16_f32 v22, v104, v105
	v_cvt_pk_bf16_f32 v23, v106, v107
	ds_write_b128 v24, v[20:23] offset:14336
	s_waitcnt vmcnt(0)
	v_pk_mul_f32 v[108:109], v[108:109], s[44:45] op_sel_hi:[1,0]
	v_pk_mul_f32 v[110:111], v[110:111], s[44:45] op_sel_hi:[1,0]
	v_pk_mul_f32 v[112:113], v[112:113], s[44:45] op_sel_hi:[1,0]
	v_pk_mul_f32 v[114:115], v[114:115], s[44:45] op_sel_hi:[1,0]
	v_cvt_pk_bf16_f32 v12, v108, v109
	v_cvt_pk_bf16_f32 v13, v110, v111
	v_cvt_pk_bf16_f32 v14, v112, v113
	v_cvt_pk_bf16_f32 v15, v114, v115
	ds_write_b128 v25, v[12:15] offset:15360
	v_lshrrev_b32_e32 v29, 6, v0
	s_mov_b32 s51, s30
	v_readfirstlane_b32 s50, v29
	s_add_i32 s52, s24, s31
	s_mov_b32 s54, s32
	s_mov_b32 s55, s33
	s_lshl_b32 s43, s30, 16
	s_add_i32 s56, s43, 0x4000
	s_add_u32 s74, s34, 0x10000
	s_addc_u32 s75, s35, 0
	s_mov_b32 s76, s26
	s_mov_b32 s77, s27
	s_add_i32 s61, s28, s43
	s_add_i32 s43, s30, 1
	s_and_b32 s43, s43, 7
	s_lshl_b32 s43, s43, 16
	s_add_i32 s62, s28, s43
	s_add_i32 s43, s30, 2
	s_and_b32 s43, s43, 7
	s_lshl_b32 s43, s43, 16
	s_add_i32 s63, s28, s43
	s_add_i32 s43, s30, 3
	s_and_b32 s43, s43, 7
	s_lshl_b32 s43, s43, 16
	s_add_i32 s87, s28, s43
	s_add_i32 s43, s30, 7
	s_and_b32 s43, s43, 7
	s_lshl_b32 s43, s43, 16
	s_add_i32 s88, s28, s43
	s_add_i32 s88, s88, 0xc000
	s_mov_b32 s58, s87
	s_mov_b32 s57, s63
	s_mov_b32 s59, 0x10000
	s_mov_b32 s60, 0x10000
	s_lshl_b32 s43, s50, 11
	s_add_i32 s84, s43, 0x24000
	s_add_i32 s85, s84, 0x3f0
	s_mov_b32 s64, s10
	s_mov_b32 s65, s11
	s_mov_b32 s66, 0x10000
	s_mov_b32 s67, 0x4000
	s_mov_b32 s68, 0xc000
	s_mov_b32 s69, 0x14000
	s_mov_b32 s70, 0x600df1a6
	s_mov_b32 s71, 0x155510
	s_mov_b32 s72, s46
	s_mov_b32 s73, s47
	s_mov_b32 s53, 0x10000
	v_mov_b32_e32 v208, v2
	v_lshlrev_b32_e32 v41, 2, v39
	v_and_b32_e32 v41, 28, v41
	v_mov_b32_e32 v209, v41
	s_waitcnt vmcnt(0)
	s_barrier
	v_cmp_eq_u32_e32 vcc, 0, v0
	s_and_saveexec_b64 s[38:39], vcc
	s_cbranch_execz .Lpro_noflag
	v_mov_b32_e32 v12, 0x600df1a6
	v_mov_b32_e32 v13, 0
	global_store_dword v13, v12, s[46:47] sc1
.Lpro_noflag:
	s_or_b64 exec, exec, s[38:39]
	v_bfe_u32 v3, v0, 5, 1
	v_lshlrev_b32_e32 v4, 8, v0
	v_and_b32_e32 v4, 0x1f00, v4
	v_and_b32_e32 v5, 7, v0
	v_bitop3_b32 v6, v3, v0, 7 bitop3:0x78
	v_lshl_or_b32 v64, v6, 4, v4
	v_bitop3_b32 v6, v3, v5, 2 bitop3:0x36
	v_lshl_or_b32 v65, v6, 4, v4
	v_bitop3_b32 v6, v3, v5, 4 bitop3:0x36
	v_bitop3_b32 v5, v3, v5, 6 bitop3:0x36
	v_lshl_or_b32 v66, v6, 4, v4
	v_lshl_or_b32 v67, v5, 4, v4
	v_and_b32_e32 v4, 3, v0
	v_lshlrev_b32_e32 v6, 4, v0
	v_lshlrev_b32_e32 v5, 3, v4
	v_and_b32_e32 v6, 0xc0, v6
	v_lshlrev_b32_e32 v8, 1, v0
	v_lshlrev_b32_e32 v9, 8, v3
	v_bfe_u32 v7, v0, 4, 2
	v_and_b32_e32 v8, 32, v8
	v_or3_b32 v5, v5, v9, v6
	s_mov_b32 s0, 0x8000
	v_or3_b32 v184, v5, v8, s0
	v_lshlrev_b32_e32 v5, 8, v7
	v_xor_b32_e32 v6, v7, v1
	s_cmp_lg_u32 0, -1
	v_lshl_or_b32 v222, v6, 4, v5
	v_bitop3_b32 v1, v7, v1, 4 bitop3:0x36
	s_mov_b32 m0, s29
	s_nop 0
	buffer_load_dwordx4 v222, s[12:15], s61 offen lds
	s_cselect_b32 s17, 0, 0
	v_lshl_or_b32 v223, v1, 4, v5
	s_add_i32 s20, s29, 0x400
	s_add_i32 s0, s61, 0x400
	s_mov_b32 m0, s20
	s_nop 0
	buffer_load_dwordx4 v223, s[12:15], s0 offen lds
	v_lshlrev_b32_e32 v0, 6, v0
	s_add_i32 s21, s29, 0x800
	s_add_i32 s0, s61, 0x800
	s_mov_b32 m0, s21
	s_nop 0
	buffer_load_dwordx4 v222, s[12:15], s0 offen lds
	v_and_b32_e32 v0, 0x700, v0
	v_lshlrev_b32_e32 v1, 6, v3
	v_lshlrev_b32_e32 v3, 4, v4
	s_add_i32 s22, s29, 0xc00
	s_add_i32 s1, s61, 0xc00
	s_mov_b32 m0, s22
	s_nop 0
	buffer_load_dwordx4 v223, s[12:15], s1 offen lds
	v_or3_b32 v196, v0, v1, v3
	s_add_i32 s2, s29, 0x8000
	s_mov_b32 m0, s2
	s_nop 0
	buffer_load_dwordx4 v196, s[4:7], s61 offen lds
	s_add_i32 s1, s2, 0x400
	s_add_i32 s3, s61, 0x80
	s_mov_b32 m0, s1
	s_nop 0
	buffer_load_dwordx4 v196, s[4:7], s3 offen lds
	s_add_i32 s1, s2, 0x800
	s_mov_b32 m0, s1
	s_nop 0
	buffer_load_dwordx4 v196, s[4:7], s0 offen lds
	s_add_i32 s0, s2, 0xc00
	s_add_i32 s1, s61, 0x880
	s_mov_b32 m0, s0
	s_nop 0
	buffer_load_dwordx4 v196, s[4:7], s1 offen lds
	v_or_b32_e32 v2, 0x10000, v40
	v_add_u32_e32 v218, s17, v64
	v_add_u32_e32 v219, s17, v65
	v_add_u32_e32 v220, s17, v66
	v_add_u32_e32 v221, s17, v67
	v_add_u32_e32 v32, v2, v218
	v_add_u32_e32 v33, v2, v219
	v_add_u32_e32 v34, v2, v220
	v_add_u32_e32 v35, v2, v221
	v_add_u32_e32 v212, s17, v184
	global_load_dword v38, v41, s[64:65] sc1
	s_mov_b32 m0, s84
	s_nop 0
	buffer_load_dwordx4 v208, s[80:83], s86 offen lds
	s_mov_b32 m0, s85
	s_nop 0
	buffer_load_dwordx4 v208, s[80:83], s86 offen offset:16 lds
	s_add_i32 s86, s86, 0x2000
	s_waitcnt lgkmcnt(0)
	ds_read_b128 v[0:3], v32 offset:0
	ds_read_b128 v[4:7], v33 offset:0
	ds_read_b128 v[8:11], v34 offset:0
	ds_read_b128 v[12:15], v35 offset:0
	ds_read_b128 v[16:19], v32 offset:128
	ds_read_b128 v[20:23], v33 offset:128
	ds_read_b128 v[24:27], v34 offset:128
	ds_read_b128 v[28:31], v35 offset:128
	s_waitcnt lgkmcnt(0)
	v_accvgpr_write_b32 a[128], v0
	v_accvgpr_write_b32 a[129], v1
	v_accvgpr_write_b32 a[130], v2
	v_accvgpr_write_b32 a[131], v3
	v_accvgpr_write_b32 a[132], v4
	v_accvgpr_write_b32 a[133], v5
	v_accvgpr_write_b32 a[134], v6
	v_accvgpr_write_b32 a[135], v7
	v_accvgpr_write_b32 a[136], v8
	v_accvgpr_write_b32 a[137], v9
	v_accvgpr_write_b32 a[138], v10
	v_accvgpr_write_b32 a[139], v11
	v_accvgpr_write_b32 a[140], v12
	v_accvgpr_write_b32 a[141], v13
	v_accvgpr_write_b32 a[142], v14
	v_accvgpr_write_b32 a[143], v15
	v_accvgpr_write_b32 a[144], v16
	v_accvgpr_write_b32 a[145], v17
	v_accvgpr_write_b32 a[146], v18
	v_accvgpr_write_b32 a[147], v19
	v_accvgpr_write_b32 a[148], v20
	v_accvgpr_write_b32 a[149], v21
	v_accvgpr_write_b32 a[150], v22
	v_accvgpr_write_b32 a[151], v23
	v_accvgpr_write_b32 a[152], v24
	v_accvgpr_write_b32 a[153], v25
	v_accvgpr_write_b32 a[154], v26
	v_accvgpr_write_b32 a[155], v27
	v_accvgpr_write_b32 a[156], v28
	v_accvgpr_write_b32 a[157], v29
	v_accvgpr_write_b32 a[158], v30
	v_accvgpr_write_b32 a[159], v31
	ds_read_b128 v[0:3], v32 offset:8192
	ds_read_b128 v[4:7], v33 offset:8192
	ds_read_b128 v[8:11], v34 offset:8192
	ds_read_b128 v[12:15], v35 offset:8192
	ds_read_b128 v[16:19], v32 offset:8320
	ds_read_b128 v[20:23], v33 offset:8320
	ds_read_b128 v[24:27], v34 offset:8320
	ds_read_b128 v[28:31], v35 offset:8320
	s_waitcnt lgkmcnt(0)
	v_accvgpr_write_b32 a[160], v0
	v_accvgpr_write_b32 a[161], v1
	v_accvgpr_write_b32 a[162], v2
	v_accvgpr_write_b32 a[163], v3
	v_accvgpr_write_b32 a[164], v4
	v_accvgpr_write_b32 a[165], v5
	v_accvgpr_write_b32 a[166], v6
	v_accvgpr_write_b32 a[167], v7
	v_accvgpr_write_b32 a[168], v8
	v_accvgpr_write_b32 a[169], v9
	v_accvgpr_write_b32 a[170], v10
	v_accvgpr_write_b32 a[171], v11
	v_accvgpr_write_b32 a[172], v12
	v_accvgpr_write_b32 a[173], v13
	v_accvgpr_write_b32 a[174], v14
	v_accvgpr_write_b32 a[175], v15
	v_accvgpr_write_b32 a[176], v16
	v_accvgpr_write_b32 a[177], v17
	v_accvgpr_write_b32 a[178], v18
	v_accvgpr_write_b32 a[179], v19
	v_accvgpr_write_b32 a[180], v20
	v_accvgpr_write_b32 a[181], v21
	v_accvgpr_write_b32 a[182], v22
	v_accvgpr_write_b32 a[183], v23
	v_accvgpr_write_b32 a[184], v24
	v_accvgpr_write_b32 a[185], v25
	v_accvgpr_write_b32 a[186], v26
	v_accvgpr_write_b32 a[187], v27
	v_accvgpr_write_b32 a[188], v28
	v_accvgpr_write_b32 a[189], v29
	v_accvgpr_write_b32 a[190], v30
	v_accvgpr_write_b32 a[191], v31
	s_waitcnt vmcnt(0) lgkmcnt(0)
	s_barrier
	s_nop 0
	ds_read_b128 a[192:195], v218 offset:0
	s_nop 0
	ds_read_b128 a[196:199], v219 offset:0
	ds_read_b128 a[200:203], v220 offset:0
	ds_read_b128 a[204:207], v221 offset:0
	ds_read_b128 a[208:211], v218 offset:128
	ds_read_b128 a[212:215], v219 offset:128
	ds_read_b128 a[216:219], v220 offset:128
	ds_read_b128 a[220:223], v221 offset:128
	ds_read_b128 a[224:227], v218 offset:8192
	ds_read_b128 a[228:231], v219 offset:8192
	ds_read_b128 a[232:235], v220 offset:8192
	ds_read_b128 a[236:239], v221 offset:8192
	ds_read_b128 a[240:243], v218 offset:8320
	ds_read_b128 a[244:247], v219 offset:8320
	ds_read_b128 a[248:251], v220 offset:8320
	ds_read_b128 a[252:255], v221 offset:8320
	s_waitcnt lgkmcnt(0)
	s_nop 0
	s_waitcnt vmcnt(0)
	v_cmp_eq_u32_e32 vcc, s70, v38
	s_cmp_eq_u64 vcc, exec
	s_cbranch_scc0 .LBB0_27
